# P3 lora epilogue: bias vectors loaded once per unit instead of per row group behind vmcnt(0)
# baseline (speedup 1.0000x reference)
;     __device__ __forceinline__ void operator()(const f32x4 (&acc)[2][2][4][2], const Unit& u, int wr, int wc, int fr_, int fq_) const {
;     ...
;         const int mode = u.pn >> 3; float* base = WDEC + (size_t)mode * ((size_t)8192 * 2048);
;         bf16_t* baseh = (bf16_t*)base;
;         const int row0 = u.pm * BM + wr * 64 + fr, col0 = (u.pn & 7) * BM + wc * 32 + 8 * fq;
;         const float* bp = mode == 0 ? w0 : a0;
; #pragma unroll
;         for (int ai = 0; ai < 2; ++ai)
; #pragma unroll
;             for (int m = 0; m < 4; ++m) { const size_t ro = (size_t)(row0 + ai * HALF + m * 16) * 2048 + col0;
; #pragma unroll
;                 for (int bj = 0; bj < 2; ++bj) { f32x4 v0 = acc[ai][bj][m][0], v1 = acc[ai][bj][m][1];
;                     if (mode < 2) { v0 += *(const f32x4*)(bp + col0 + bj * HALF); v1 += *(const f32x4*)(bp + col0 + bj * HALF + 4); }
.LBB0_1597:
	s_lshl_b32 s4, s90, 8
	s_and_b32 s4, s4, 0x700
	s_ashr_i32 s8, s90, 3
	s_or_b32 s4, s4, s54
	v_mbcnt_lo_u32_b32 v158, -1, 0
	v_mbcnt_hi_u32_b32 v158, -1, v158
	s_cmp_gt_u32 s90, 7
	v_ashrrev_i32_e32 v130, 1, v158
	v_and_b32_e32 v130, -8, v130
	s_cselect_b64 s[10:11], -1, 0
	s_cmp_lt_u32 s90, 8
	v_add_u32_e32 v156, s4, v130
	s_cselect_b32 s4, s45, s49
	s_cselect_b32 s5, s44, s48
	v_mov_b32_e32 v130, s5
	v_mov_b32_e32 v131, s4
	v_ashrrev_i32_e32 v157, 31, v156
	s_cmp_lt_i32 s8, 2
	s_cselect_b64 s[92:93], -1, 0
	s_cmp_gt_i32 s8, 1
	v_lshl_add_u64 v[154:155], v[156:157], 2, v[130:131]
	s_cbranch_scc1 .LBB0_1599
	global_load_dwordx4 v[130:133], v[154:155], off
	global_load_dwordx4 v[134:137], v[154:155], off offset:16
	s_waitcnt vmcnt(0)
	v_mov_b64_e32 v[170:171], v[130:131]
	v_mov_b64_e32 v[172:173], v[132:133]
	v_mov_b64_e32 v[174:175], v[134:135]
	v_mov_b64_e32 v[176:177], v[136:137]
	v_pk_add_f32 v[128:129], v[128:129], v[132:133]
	v_pk_add_f32 v[126:127], v[126:127], v[130:131]
	v_pk_add_f32 v[124:125], v[124:125], v[136:137]
	v_pk_add_f32 v[122:123], v[122:123], v[134:135]

;     __device__ __forceinline__ void operator()(const f32x4 (&acc)[2][2][4][2], const Unit& u, int wr, int wc, int fr_, int fq_) const {
;     ...
;                     if (mode < 2) { v0 += *(const f32x4*)(bp + col0 + bj * HALF); v1 += *(const f32x4*)(bp + col0 + bj * HALF + 4); }
.LBB0_1608:
	global_load_dwordx4 v[122:125], v[154:155], off offset:512
	global_load_dwordx4 v[126:129], v[154:155], off offset:528
	s_waitcnt vmcnt(0)
	v_mov_b64_e32 v[178:179], v[122:123]
	v_mov_b64_e32 v[180:181], v[124:125]
	v_mov_b64_e32 v[182:183], v[126:127]
	v_mov_b64_e32 v[184:185], v[128:129]
	v_pk_add_f32 v[120:121], v[120:121], v[124:125]
	v_pk_add_f32 v[118:119], v[118:119], v[122:123]
	v_pk_add_f32 v[116:117], v[116:117], v[128:129]
	v_pk_add_f32 v[114:115], v[114:115], v[126:127]

;     __device__ __forceinline__ void operator()(const f32x4 (&acc)[2][2][4][2], const Unit& u, int wr, int wc, int fr_, int fq_) const {
;     ...
;                     if (mode < 2) { v0 += *(const f32x4*)(bp + col0 + bj * HALF); v1 += *(const f32x4*)(bp + col0 + bj * HALF + 4); }
.LBB0_1621:
	s_and_b64 vcc, exec, s[8:9]
	s_cbranch_vccnz .LBB0_1623
	v_mov_b64_e32 v[114:115], v[170:171]
	v_mov_b64_e32 v[116:117], v[172:173]
	v_mov_b64_e32 v[118:119], v[174:175]
	v_mov_b64_e32 v[120:121], v[176:177]
	v_pk_add_f32 v[112:113], v[112:113], v[116:117]
	v_pk_add_f32 v[110:111], v[110:111], v[114:115]
	v_pk_add_f32 v[108:109], v[108:109], v[120:121]
	v_pk_add_f32 v[106:107], v[106:107], v[118:119]

;     __device__ __forceinline__ void operator()(const f32x4 (&acc)[2][2][4][2], const Unit& u, int wr, int wc, int fr_, int fq_) const {
;     ...
;                     if (mode < 2) { v0 += *(const f32x4*)(bp + col0 + bj * HALF); v1 += *(const f32x4*)(bp + col0 + bj * HALF + 4); }
.LBB0_1632:
	v_mov_b64_e32 v[106:107], v[178:179]
	v_mov_b64_e32 v[108:109], v[180:181]
	v_mov_b64_e32 v[110:111], v[182:183]
	v_mov_b64_e32 v[112:113], v[184:185]
	v_pk_add_f32 v[104:105], v[104:105], v[108:109]
	v_pk_add_f32 v[102:103], v[102:103], v[106:107]
	v_pk_add_f32 v[100:101], v[100:101], v[112:113]
	v_pk_add_f32 v[98:99], v[98:99], v[110:111]

;     __device__ __forceinline__ void operator()(const f32x4 (&acc)[2][2][4][2], const Unit& u, int wr, int wc, int fr_, int fq_) const {
;     ...
;                     if (mode < 2) { v0 += *(const f32x4*)(bp + col0 + bj * HALF); v1 += *(const f32x4*)(bp + col0 + bj * HALF + 4); }
.LBB0_1645:
	s_and_b64 vcc, exec, s[8:9]
	s_cbranch_vccnz .LBB0_1647
	v_mov_b64_e32 v[98:99], v[170:171]
	v_mov_b64_e32 v[100:101], v[172:173]
	v_mov_b64_e32 v[102:103], v[174:175]
	v_mov_b64_e32 v[104:105], v[176:177]
	v_pk_add_f32 v[96:97], v[96:97], v[100:101]
	v_pk_add_f32 v[94:95], v[94:95], v[98:99]
	v_pk_add_f32 v[92:93], v[92:93], v[104:105]
	v_pk_add_f32 v[90:91], v[90:91], v[102:103]

;     __device__ __forceinline__ void operator()(const f32x4 (&acc)[2][2][4][2], const Unit& u, int wr, int wc, int fr_, int fq_) const {
;     ...
;                     if (mode < 2) { v0 += *(const f32x4*)(bp + col0 + bj * HALF); v1 += *(const f32x4*)(bp + col0 + bj * HALF + 4); }
.LBB0_1656:
	v_mov_b64_e32 v[90:91], v[178:179]
	v_mov_b64_e32 v[92:93], v[180:181]
	v_mov_b64_e32 v[94:95], v[182:183]
	v_mov_b64_e32 v[96:97], v[184:185]
	v_pk_add_f32 v[88:89], v[88:89], v[92:93]
	v_pk_add_f32 v[86:87], v[86:87], v[90:91]
	v_pk_add_f32 v[84:85], v[84:85], v[96:97]
	v_pk_add_f32 v[82:83], v[82:83], v[94:95]

;     __device__ __forceinline__ void operator()(const f32x4 (&acc)[2][2][4][2], const Unit& u, int wr, int wc, int fr_, int fq_) const {
;     ...
;                     if (mode < 2) { v0 += *(const f32x4*)(bp + col0 + bj * HALF); v1 += *(const f32x4*)(bp + col0 + bj * HALF + 4); }
.LBB0_1669:
	s_and_b64 vcc, exec, s[8:9]
	s_cbranch_vccnz .LBB0_1671
	v_mov_b64_e32 v[82:83], v[170:171]
	v_mov_b64_e32 v[84:85], v[172:173]
	v_mov_b64_e32 v[86:87], v[174:175]
	v_mov_b64_e32 v[88:89], v[176:177]
	v_pk_add_f32 v[80:81], v[80:81], v[84:85]
	v_pk_add_f32 v[78:79], v[78:79], v[82:83]
	v_pk_add_f32 v[76:77], v[76:77], v[88:89]
	v_pk_add_f32 v[74:75], v[74:75], v[86:87]

;     __device__ __forceinline__ void operator()(const f32x4 (&acc)[2][2][4][2], const Unit& u, int wr, int wc, int fr_, int fq_) const {
;     ...
;                     if (mode < 2) { v0 += *(const f32x4*)(bp + col0 + bj * HALF); v1 += *(const f32x4*)(bp + col0 + bj * HALF + 4); }
.LBB0_1680:
	v_mov_b64_e32 v[74:75], v[178:179]
	v_mov_b64_e32 v[76:77], v[180:181]
	v_mov_b64_e32 v[78:79], v[182:183]
	v_mov_b64_e32 v[80:81], v[184:185]
	v_pk_add_f32 v[72:73], v[72:73], v[76:77]
	v_pk_add_f32 v[70:71], v[70:71], v[74:75]
	v_pk_add_f32 v[68:69], v[68:69], v[80:81]
	v_pk_add_f32 v[66:67], v[66:67], v[78:79]

;     __device__ __forceinline__ void operator()(const f32x4 (&acc)[2][2][4][2], const Unit& u, int wr, int wc, int fr_, int fq_) const {
;     ...
;                     if (mode < 2) { v0 += *(const f32x4*)(bp + col0 + bj * HALF); v1 += *(const f32x4*)(bp + col0 + bj * HALF + 4); }
.LBB0_1693:
	s_and_b64 vcc, exec, s[8:9]
	s_cbranch_vccnz .LBB0_1695
	v_mov_b64_e32 v[66:67], v[170:171]
	v_mov_b64_e32 v[68:69], v[172:173]
	v_mov_b64_e32 v[70:71], v[174:175]
	v_mov_b64_e32 v[72:73], v[176:177]
	v_pk_add_f32 v[64:65], v[64:65], v[68:69]
	v_pk_add_f32 v[62:63], v[62:63], v[66:67]
	v_pk_add_f32 v[60:61], v[60:61], v[72:73]
	v_pk_add_f32 v[58:59], v[58:59], v[70:71]

;     __device__ __forceinline__ void operator()(const f32x4 (&acc)[2][2][4][2], const Unit& u, int wr, int wc, int fr_, int fq_) const {
;     ...
;                     if (mode < 2) { v0 += *(const f32x4*)(bp + col0 + bj * HALF); v1 += *(const f32x4*)(bp + col0 + bj * HALF + 4); }
.LBB0_1704:
	v_mov_b64_e32 v[58:59], v[178:179]
	v_mov_b64_e32 v[60:61], v[180:181]
	v_mov_b64_e32 v[62:63], v[182:183]
	v_mov_b64_e32 v[64:65], v[184:185]
	v_pk_add_f32 v[56:57], v[56:57], v[60:61]
	v_pk_add_f32 v[54:55], v[54:55], v[58:59]
	v_pk_add_f32 v[52:53], v[52:53], v[64:65]
	v_pk_add_f32 v[50:51], v[50:51], v[62:63]

;     __device__ __forceinline__ void operator()(const f32x4 (&acc)[2][2][4][2], const Unit& u, int wr, int wc, int fr_, int fq_) const {
;     ...
;                     if (mode < 2) { v0 += *(const f32x4*)(bp + col0 + bj * HALF); v1 += *(const f32x4*)(bp + col0 + bj * HALF + 4); }
.LBB0_1717:
	s_and_b64 vcc, exec, s[8:9]
	s_cbranch_vccnz .LBB0_1719
	v_mov_b64_e32 v[50:51], v[170:171]
	v_mov_b64_e32 v[52:53], v[172:173]
	v_mov_b64_e32 v[54:55], v[174:175]
	v_mov_b64_e32 v[56:57], v[176:177]
	v_pk_add_f32 v[48:49], v[48:49], v[52:53]
	v_pk_add_f32 v[46:47], v[46:47], v[50:51]
	v_pk_add_f32 v[44:45], v[44:45], v[56:57]
	v_pk_add_f32 v[42:43], v[42:43], v[54:55]

;     __device__ __forceinline__ void operator()(const f32x4 (&acc)[2][2][4][2], const Unit& u, int wr, int wc, int fr_, int fq_) const {
;     ...
;                     if (mode < 2) { v0 += *(const f32x4*)(bp + col0 + bj * HALF); v1 += *(const f32x4*)(bp + col0 + bj * HALF + 4); }
.LBB0_1728:
	v_mov_b64_e32 v[42:43], v[178:179]
	v_mov_b64_e32 v[44:45], v[180:181]
	v_mov_b64_e32 v[46:47], v[182:183]
	v_mov_b64_e32 v[48:49], v[184:185]
	v_pk_add_f32 v[40:41], v[40:41], v[44:45]
	v_pk_add_f32 v[38:39], v[38:39], v[42:43]
	v_pk_add_f32 v[36:37], v[36:37], v[48:49]
	v_pk_add_f32 v[34:35], v[34:35], v[46:47]

;     __device__ __forceinline__ void operator()(const f32x4 (&acc)[2][2][4][2], const Unit& u, int wr, int wc, int fr_, int fq_) const {
;     ...
;                     if (mode < 2) { v0 += *(const f32x4*)(bp + col0 + bj * HALF); v1 += *(const f32x4*)(bp + col0 + bj * HALF + 4); }
.LBB0_1741:
	s_and_b64 vcc, exec, s[8:9]
	s_cbranch_vccnz .LBB0_1743
	v_mov_b64_e32 v[34:35], v[170:171]
	v_mov_b64_e32 v[36:37], v[172:173]
	v_mov_b64_e32 v[38:39], v[174:175]
	v_mov_b64_e32 v[40:41], v[176:177]
	v_pk_add_f32 v[32:33], v[32:33], v[36:37]
	v_pk_add_f32 v[30:31], v[30:31], v[34:35]
	v_pk_add_f32 v[28:29], v[28:29], v[40:41]
	v_pk_add_f32 v[26:27], v[26:27], v[38:39]

;     __device__ __forceinline__ void operator()(const f32x4 (&acc)[2][2][4][2], const Unit& u, int wr, int wc, int fr_, int fq_) const {
;     ...
;                     if (mode < 2) { v0 += *(const f32x4*)(bp + col0 + bj * HALF); v1 += *(const f32x4*)(bp + col0 + bj * HALF + 4); }
.LBB0_1752:
	v_mov_b64_e32 v[26:27], v[178:179]
	v_mov_b64_e32 v[28:29], v[180:181]
	v_mov_b64_e32 v[30:31], v[182:183]
	v_mov_b64_e32 v[32:33], v[184:185]
	v_pk_add_f32 v[24:25], v[24:25], v[28:29]
	v_pk_add_f32 v[22:23], v[22:23], v[26:27]
	v_pk_add_f32 v[20:21], v[20:21], v[32:33]
	v_pk_add_f32 v[18:19], v[18:19], v[30:31]

;     __device__ __forceinline__ void operator()(const f32x4 (&acc)[2][2][4][2], const Unit& u, int wr, int wc, int fr_, int fq_) const {
;     ...
;                     if (mode < 2) { v0 += *(const f32x4*)(bp + col0 + bj * HALF); v1 += *(const f32x4*)(bp + col0 + bj * HALF + 4); }
.LBB0_1765:
	s_and_b64 vcc, exec, s[8:9]
	s_cbranch_vccnz .LBB0_1767
	v_mov_b64_e32 v[18:19], v[170:171]
	v_mov_b64_e32 v[20:21], v[172:173]
	v_mov_b64_e32 v[22:23], v[174:175]
	v_mov_b64_e32 v[24:25], v[176:177]
	v_pk_add_f32 v[16:17], v[16:17], v[20:21]
	v_pk_add_f32 v[14:15], v[14:15], v[18:19]
	v_pk_add_f32 v[12:13], v[12:13], v[24:25]
	v_pk_add_f32 v[10:11], v[10:11], v[22:23]

;     __device__ __forceinline__ void operator()(const f32x4 (&acc)[2][2][4][2], const Unit& u, int wr, int wc, int fr_, int fq_) const {
;     ...
;                 for (int bj = 0; bj < 2; ++bj) { f32x4 v0 = acc[ai][bj][m][0], v1 = acc[ai][bj][m][1];
;                     if (mode < 2) { v0 += *(const f32x4*)(bp + col0 + bj * HALF); v1 += *(const f32x4*)(bp + col0 + bj * HALF + 4); }
.LBB0_1776:
	v_mov_b64_e32 v[10:11], v[178:179]
	v_mov_b64_e32 v[12:13], v[180:181]
	v_mov_b64_e32 v[14:15], v[182:183]
	v_mov_b64_e32 v[16:17], v[184:185]
	v_pk_add_f32 v[8:9], v[8:9], v[12:13]
	v_pk_add_f32 v[6:7], v[6:7], v[10:11]
	v_pk_add_f32 v[4:5], v[4:5], v[16:17]
	v_pk_add_f32 v[2:3], v[2:3], v[14:15]
